# P4 stabiliser scan: the 8 serial threads only run m = max(g+m, mloc); decay/scale expf and m_prev stores done by all 512 threads after a barrier
# baseline (speedup 1.0000x reference)
.LBB0_681:
	v_ashrrev_i32_e32 v53, 31, v52
	v_lshl_add_u64 v[0:1], v[52:53], 2, s[92:93]
	v_add_co_u32_e32 v0, vcc, 0x35e0000, v0
	s_waitcnt lgkmcnt(0)
	s_nop 0
	v_addc_co_u32_e32 v1, vcc, 0, v1, vcc
	s_barrier
	global_load_dword v2, v[0:1], off offset:1024
	global_load_dword v3, v[0:1], off offset:3072
	v_lshl_add_u32 v0, v52, 2, 0
	v_cmp_gt_i32_e32 vcc, 8, v52
	s_waitcnt vmcnt(0)
	ds_write2st64_b32 v0, v2, v3 offset0:16 offset1:24
	s_waitcnt lgkmcnt(0)
	s_barrier
	s_and_saveexec_b64 s[0:1], vcc
	s_cbranch_execz .Lp4_ms_done
	v_lshlrev_b32_e32 v0, 8, v52
	v_mov_b32_e32 v6, 0
	ds_read_b128 v[8:11], v0 offset:4096
	ds_read_b128 v[12:15], v0 offset:6144
	s_waitcnt lgkmcnt(0)
	ds_write_b32 v0, v6 offset:0
	v_add_f32_e32 v4, v6, v8
	v_max_f32_e32 v5, v12, v12
	v_max_f32_e32 v6, v4, v5
	ds_write_b32 v0, v6 offset:4
	v_add_f32_e32 v4, v6, v9
	v_max_f32_e32 v5, v13, v13
	v_max_f32_e32 v6, v4, v5
	ds_write_b32 v0, v6 offset:8
	v_add_f32_e32 v4, v6, v10
	v_max_f32_e32 v5, v14, v14
	v_max_f32_e32 v6, v4, v5
	ds_write_b32 v0, v6 offset:12
	v_add_f32_e32 v4, v6, v11
	v_max_f32_e32 v5, v15, v15
	v_max_f32_e32 v6, v4, v5
	ds_read_b128 v[8:11], v0 offset:4112
	ds_read_b128 v[12:15], v0 offset:6160
	s_waitcnt lgkmcnt(0)
	ds_write_b32 v0, v6 offset:16
	v_add_f32_e32 v4, v6, v8
	v_max_f32_e32 v5, v12, v12
	v_max_f32_e32 v6, v4, v5
	ds_write_b32 v0, v6 offset:20
	v_add_f32_e32 v4, v6, v9
	v_max_f32_e32 v5, v13, v13
	v_max_f32_e32 v6, v4, v5
	ds_write_b32 v0, v6 offset:24
	v_add_f32_e32 v4, v6, v10
	v_max_f32_e32 v5, v14, v14
	v_max_f32_e32 v6, v4, v5
	ds_write_b32 v0, v6 offset:28
	v_add_f32_e32 v4, v6, v11
	v_max_f32_e32 v5, v15, v15
	v_max_f32_e32 v6, v4, v5
	ds_read_b128 v[8:11], v0 offset:4128
	ds_read_b128 v[12:15], v0 offset:6176
	s_waitcnt lgkmcnt(0)
	ds_write_b32 v0, v6 offset:32
	v_add_f32_e32 v4, v6, v8
	v_max_f32_e32 v5, v12, v12
	v_max_f32_e32 v6, v4, v5
	ds_write_b32 v0, v6 offset:36
	v_add_f32_e32 v4, v6, v9
	v_max_f32_e32 v5, v13, v13
	v_max_f32_e32 v6, v4, v5
	ds_write_b32 v0, v6 offset:40
	v_add_f32_e32 v4, v6, v10
	v_max_f32_e32 v5, v14, v14
	v_max_f32_e32 v6, v4, v5
	ds_write_b32 v0, v6 offset:44
	v_add_f32_e32 v4, v6, v11
	v_max_f32_e32 v5, v15, v15
	v_max_f32_e32 v6, v4, v5
	ds_read_b128 v[8:11], v0 offset:4144
	ds_read_b128 v[12:15], v0 offset:6192
	s_waitcnt lgkmcnt(0)
	ds_write_b32 v0, v6 offset:48
	v_add_f32_e32 v4, v6, v8
	v_max_f32_e32 v5, v12, v12
	v_max_f32_e32 v6, v4, v5
	ds_write_b32 v0, v6 offset:52
	v_add_f32_e32 v4, v6, v9
	v_max_f32_e32 v5, v13, v13
	v_max_f32_e32 v6, v4, v5
	ds_write_b32 v0, v6 offset:56
	v_add_f32_e32 v4, v6, v10
	v_max_f32_e32 v5, v14, v14
	v_max_f32_e32 v6, v4, v5
	ds_write_b32 v0, v6 offset:60
	v_add_f32_e32 v4, v6, v11
	v_max_f32_e32 v5, v15, v15
	v_max_f32_e32 v6, v4, v5
	ds_read_b128 v[8:11], v0 offset:4160
	ds_read_b128 v[12:15], v0 offset:6208
	s_waitcnt lgkmcnt(0)
	ds_write_b32 v0, v6 offset:64
	v_add_f32_e32 v4, v6, v8
	v_max_f32_e32 v5, v12, v12
	v_max_f32_e32 v6, v4, v5
	ds_write_b32 v0, v6 offset:68
	v_add_f32_e32 v4, v6, v9
	v_max_f32_e32 v5, v13, v13
	v_max_f32_e32 v6, v4, v5
	ds_write_b32 v0, v6 offset:72
	v_add_f32_e32 v4, v6, v10
	v_max_f32_e32 v5, v14, v14
	v_max_f32_e32 v6, v4, v5
	ds_write_b32 v0, v6 offset:76
	v_add_f32_e32 v4, v6, v11
	v_max_f32_e32 v5, v15, v15
	v_max_f32_e32 v6, v4, v5
	ds_read_b128 v[8:11], v0 offset:4176
	ds_read_b128 v[12:15], v0 offset:6224
	s_waitcnt lgkmcnt(0)
	ds_write_b32 v0, v6 offset:80
	v_add_f32_e32 v4, v6, v8
	v_max_f32_e32 v5, v12, v12
	v_max_f32_e32 v6, v4, v5
	ds_write_b32 v0, v6 offset:84
	v_add_f32_e32 v4, v6, v9
	v_max_f32_e32 v5, v13, v13
	v_max_f32_e32 v6, v4, v5
	ds_write_b32 v0, v6 offset:88
	v_add_f32_e32 v4, v6, v10
	v_max_f32_e32 v5, v14, v14
	v_max_f32_e32 v6, v4, v5
	ds_write_b32 v0, v6 offset:92
	v_add_f32_e32 v4, v6, v11
	v_max_f32_e32 v5, v15, v15
	v_max_f32_e32 v6, v4, v5
	ds_read_b128 v[8:11], v0 offset:4192
	ds_read_b128 v[12:15], v0 offset:6240
	s_waitcnt lgkmcnt(0)
	ds_write_b32 v0, v6 offset:96
	v_add_f32_e32 v4, v6, v8
	v_max_f32_e32 v5, v12, v12
	v_max_f32_e32 v6, v4, v5
	ds_write_b32 v0, v6 offset:100
	v_add_f32_e32 v4, v6, v9
	v_max_f32_e32 v5, v13, v13
	v_max_f32_e32 v6, v4, v5
	ds_write_b32 v0, v6 offset:104
	v_add_f32_e32 v4, v6, v10
	v_max_f32_e32 v5, v14, v14
	v_max_f32_e32 v6, v4, v5
	ds_write_b32 v0, v6 offset:108
	v_add_f32_e32 v4, v6, v11
	v_max_f32_e32 v5, v15, v15
	v_max_f32_e32 v6, v4, v5
	ds_read_b128 v[8:11], v0 offset:4208
	ds_read_b128 v[12:15], v0 offset:6256
	s_waitcnt lgkmcnt(0)
	ds_write_b32 v0, v6 offset:112
	v_add_f32_e32 v4, v6, v8
	v_max_f32_e32 v5, v12, v12
	v_max_f32_e32 v6, v4, v5
	ds_write_b32 v0, v6 offset:116
	v_add_f32_e32 v4, v6, v9
	v_max_f32_e32 v5, v13, v13
	v_max_f32_e32 v6, v4, v5
	ds_write_b32 v0, v6 offset:120
	v_add_f32_e32 v4, v6, v10
	v_max_f32_e32 v5, v14, v14
	v_max_f32_e32 v6, v4, v5
	ds_write_b32 v0, v6 offset:124
	v_add_f32_e32 v4, v6, v11
	v_max_f32_e32 v5, v15, v15
	v_max_f32_e32 v6, v4, v5
	ds_read_b128 v[8:11], v0 offset:4224
	ds_read_b128 v[12:15], v0 offset:6272
	s_waitcnt lgkmcnt(0)
	ds_write_b32 v0, v6 offset:128
	v_add_f32_e32 v4, v6, v8
	v_max_f32_e32 v5, v12, v12
	v_max_f32_e32 v6, v4, v5
	ds_write_b32 v0, v6 offset:132
	v_add_f32_e32 v4, v6, v9
	v_max_f32_e32 v5, v13, v13
	v_max_f32_e32 v6, v4, v5
	ds_write_b32 v0, v6 offset:136
	v_add_f32_e32 v4, v6, v10
	v_max_f32_e32 v5, v14, v14
	v_max_f32_e32 v6, v4, v5
	ds_write_b32 v0, v6 offset:140
	v_add_f32_e32 v4, v6, v11
	v_max_f32_e32 v5, v15, v15
	v_max_f32_e32 v6, v4, v5
	ds_read_b128 v[8:11], v0 offset:4240
	ds_read_b128 v[12:15], v0 offset:6288
	s_waitcnt lgkmcnt(0)
	ds_write_b32 v0, v6 offset:144
	v_add_f32_e32 v4, v6, v8
	v_max_f32_e32 v5, v12, v12
	v_max_f32_e32 v6, v4, v5
	ds_write_b32 v0, v6 offset:148
	v_add_f32_e32 v4, v6, v9
	v_max_f32_e32 v5, v13, v13
	v_max_f32_e32 v6, v4, v5
	ds_write_b32 v0, v6 offset:152
	v_add_f32_e32 v4, v6, v10
	v_max_f32_e32 v5, v14, v14
	v_max_f32_e32 v6, v4, v5
	ds_write_b32 v0, v6 offset:156
	v_add_f32_e32 v4, v6, v11
	v_max_f32_e32 v5, v15, v15
	v_max_f32_e32 v6, v4, v5
	ds_read_b128 v[8:11], v0 offset:4256
	ds_read_b128 v[12:15], v0 offset:6304
	s_waitcnt lgkmcnt(0)
	ds_write_b32 v0, v6 offset:160
	v_add_f32_e32 v4, v6, v8
	v_max_f32_e32 v5, v12, v12
	v_max_f32_e32 v6, v4, v5
	ds_write_b32 v0, v6 offset:164
	v_add_f32_e32 v4, v6, v9
	v_max_f32_e32 v5, v13, v13
	v_max_f32_e32 v6, v4, v5
	ds_write_b32 v0, v6 offset:168
	v_add_f32_e32 v4, v6, v10
	v_max_f32_e32 v5, v14, v14
	v_max_f32_e32 v6, v4, v5
	ds_write_b32 v0, v6 offset:172
	v_add_f32_e32 v4, v6, v11
	v_max_f32_e32 v5, v15, v15
	v_max_f32_e32 v6, v4, v5
	ds_read_b128 v[8:11], v0 offset:4272
	ds_read_b128 v[12:15], v0 offset:6320
	s_waitcnt lgkmcnt(0)
	ds_write_b32 v0, v6 offset:176
	v_add_f32_e32 v4, v6, v8
	v_max_f32_e32 v5, v12, v12
	v_max_f32_e32 v6, v4, v5
	ds_write_b32 v0, v6 offset:180
	v_add_f32_e32 v4, v6, v9
	v_max_f32_e32 v5, v13, v13
	v_max_f32_e32 v6, v4, v5
	ds_write_b32 v0, v6 offset:184
	v_add_f32_e32 v4, v6, v10
	v_max_f32_e32 v5, v14, v14
	v_max_f32_e32 v6, v4, v5
	ds_write_b32 v0, v6 offset:188
	v_add_f32_e32 v4, v6, v11
	v_max_f32_e32 v5, v15, v15
	v_max_f32_e32 v6, v4, v5
	ds_read_b128 v[8:11], v0 offset:4288
	ds_read_b128 v[12:15], v0 offset:6336
	s_waitcnt lgkmcnt(0)
	ds_write_b32 v0, v6 offset:192
	v_add_f32_e32 v4, v6, v8
	v_max_f32_e32 v5, v12, v12
	v_max_f32_e32 v6, v4, v5
	ds_write_b32 v0, v6 offset:196
	v_add_f32_e32 v4, v6, v9
	v_max_f32_e32 v5, v13, v13
	v_max_f32_e32 v6, v4, v5
	ds_write_b32 v0, v6 offset:200
	v_add_f32_e32 v4, v6, v10
	v_max_f32_e32 v5, v14, v14
	v_max_f32_e32 v6, v4, v5
	ds_write_b32 v0, v6 offset:204
	v_add_f32_e32 v4, v6, v11
	v_max_f32_e32 v5, v15, v15
	v_max_f32_e32 v6, v4, v5
	ds_read_b128 v[8:11], v0 offset:4304
	ds_read_b128 v[12:15], v0 offset:6352
	s_waitcnt lgkmcnt(0)
	ds_write_b32 v0, v6 offset:208
	v_add_f32_e32 v4, v6, v8
	v_max_f32_e32 v5, v12, v12
	v_max_f32_e32 v6, v4, v5
	ds_write_b32 v0, v6 offset:212
	v_add_f32_e32 v4, v6, v9
	v_max_f32_e32 v5, v13, v13
	v_max_f32_e32 v6, v4, v5
	ds_write_b32 v0, v6 offset:216
	v_add_f32_e32 v4, v6, v10
	v_max_f32_e32 v5, v14, v14
	v_max_f32_e32 v6, v4, v5
	ds_write_b32 v0, v6 offset:220
	v_add_f32_e32 v4, v6, v11
	v_max_f32_e32 v5, v15, v15
	v_max_f32_e32 v6, v4, v5
	ds_read_b128 v[8:11], v0 offset:4320
	ds_read_b128 v[12:15], v0 offset:6368
	s_waitcnt lgkmcnt(0)
	ds_write_b32 v0, v6 offset:224
	v_add_f32_e32 v4, v6, v8
	v_max_f32_e32 v5, v12, v12
	v_max_f32_e32 v6, v4, v5
	ds_write_b32 v0, v6 offset:228
	v_add_f32_e32 v4, v6, v9
	v_max_f32_e32 v5, v13, v13
	v_max_f32_e32 v6, v4, v5
	ds_write_b32 v0, v6 offset:232
	v_add_f32_e32 v4, v6, v10
	v_max_f32_e32 v5, v14, v14
	v_max_f32_e32 v6, v4, v5
	ds_write_b32 v0, v6 offset:236
	v_add_f32_e32 v4, v6, v11
	v_max_f32_e32 v5, v15, v15
	v_max_f32_e32 v6, v4, v5
	ds_read_b128 v[8:11], v0 offset:4336
	ds_read_b128 v[12:15], v0 offset:6384
	s_waitcnt lgkmcnt(0)
	ds_write_b32 v0, v6 offset:240
	v_add_f32_e32 v4, v6, v8
	v_max_f32_e32 v5, v12, v12
	v_max_f32_e32 v6, v4, v5
	ds_write_b32 v0, v6 offset:244
	v_add_f32_e32 v4, v6, v9
	v_max_f32_e32 v5, v13, v13
	v_max_f32_e32 v6, v4, v5
	ds_write_b32 v0, v6 offset:248
	v_add_f32_e32 v4, v6, v10
	v_max_f32_e32 v5, v14, v14
	v_max_f32_e32 v6, v4, v5
	ds_write_b32 v0, v6 offset:252
	v_add_f32_e32 v4, v6, v11
	v_max_f32_e32 v5, v15, v15
	v_max_f32_e32 v6, v4, v5
.Lp4_ms_done:
	s_or_b64 exec, exec, s[0:1]
	s_waitcnt lgkmcnt(0)
	s_barrier
	s_mov_b32 s8, 0x3fb8aa3b
	s_mov_b32 s9, 0xc2ce8ed0
	s_mov_b32 s10, 0x42b17218
	v_mov_b32_e32 v1, 0x7f800000
	v_lshlrev_b32_e32 v0, 2, v52
	ds_read_b32 v6, v0
	ds_read2st64_b32 v[4:5], v0 offset0:16 offset1:24
	s_waitcnt lgkmcnt(0)
	v_add_f32_e32 v4, v6, v4
	v_max_f32_e32 v7, v5, v5
	v_max_f32_e32 v7, v4, v7
	v_sub_f32_e32 v4, v4, v7
	v_sub_f32_e32 v5, v5, v7
	v_mul_f32_e32 v10, 0x3fb8aa3b, v4
	v_fma_f32 v8, v4, s8, -v10
	v_rndne_f32_e32 v9, v10
	v_fmac_f32_e32 v8, 0x32a5705f, v4
	v_sub_f32_e32 v10, v10, v9
	v_add_f32_e32 v10, v10, v8
	v_exp_f32_e32 v10, v10
	v_cvt_i32_f32_e32 v8, v9
	v_cmp_ngt_f32_e32 vcc, s9, v4
	v_ldexp_f32 v10, v10, v8
	s_nop 1
	v_cndmask_b32_e32 v10, 0, v10, vcc
	v_cmp_nlt_f32_e32 vcc, s10, v4
	s_nop 1
	v_cndmask_b32_e32 v10, v1, v10, vcc
	v_mul_f32_e32 v11, 0x3fb8aa3b, v5
	v_fma_f32 v8, v5, s8, -v11
	v_rndne_f32_e32 v9, v11
	v_fmac_f32_e32 v8, 0x32a5705f, v5
	v_sub_f32_e32 v11, v11, v9
	v_add_f32_e32 v11, v11, v8
	v_exp_f32_e32 v11, v11
	v_cvt_i32_f32_e32 v8, v9
	v_cmp_ngt_f32_e32 vcc, s9, v5
	v_ldexp_f32 v11, v11, v8
	s_nop 1
	v_cndmask_b32_e32 v11, 0, v11, vcc
	v_cmp_nlt_f32_e32 vcc, s10, v5
	s_nop 1
	v_cndmask_b32_e32 v11, v1, v11, vcc
	ds_write2st64_b32 v0, v10, v11 offset1:8
	s_cmp_lg_u32 s87, 0
	s_cbranch_scc1 .Lp4_ms_nostore
	v_lshl_add_u64 v[2:3], v[52:53], 2, s[92:93]
	v_add_co_u32_e32 v2, vcc, 0x35e1000, v2
	s_nop 1
	v_addc_co_u32_e32 v3, vcc, 0, v3, vcc
	global_store_dword v[2:3], v6, off offset:1024
.Lp4_ms_nostore:
.LBB0_692:
	s_or_b64 exec, exec, s[0:1]
	v_lshl_add_u32 v32, s85, 9, v52
	s_mov_b32 s0, 0x20000
	s_lshl_b32 s8, s84, 9
	v_cmp_gt_i32_e32 vcc, s0, v32
	s_waitcnt lgkmcnt(0)
	s_barrier
	s_and_saveexec_b64 s[0:1], vcc
	s_cbranch_execz .LBB0_697
	v_lshlrev_b32_e32 v0, 1, v52
	v_lshl_add_u32 v18, s85, 10, v0
	s_lshl_b32 s9, s84, 10
	s_mov_b64 s[2:3], 0
	s_mov_b32 s10, 0xfffc
	s_movk_i32 s11, 0x7fff
	s_mov_b32 s12, 0xffff0000
	s_mov_b32 s13, 0x3671000
	s_mov_b32 s14, 0x36ef1000
	s_mov_b32 s15, 0x3681000
	s_mov_b32 s16, 0x36f01000
	s_mov_b32 s17, 0x3691000
	s_mov_b32 s18, 0x36f11000
	s_mov_b32 s19, 0x36a1000
	s_mov_b32 s20, 0x36f21000
	s_mov_b32 s21, 0x36b1000
	s_mov_b32 s22, 0x36f31000
	s_mov_b32 s23, 0x36c1000
	s_mov_b32 s24, 0x36f41000
	s_mov_b32 s25, 0x36d1000
	s_mov_b32 s26, 0x36f51000
	s_mov_b32 s27, 0x1ffff
	v_mov_b32_e32 v19, v32
